# stack + static s_setprio 1 for waves 4-7 during phase C (hyena FFT units and attention), reset at the next grid barrier
# baseline (speedup 1.0000x reference)
.LBB0_607:
	s_or_b64 exec, exec, s[2:3]
	s_waitcnt lgkmcnt(0)
	s_barrier
	v_readfirstlane_b32 s32, v0
	s_nop 3
	s_bfe_u32 s32, s32, 0x40006
	s_cmp_ge_u32 s32, 4
	s_cbranch_scc0 .Lcprio_L0
	s_setprio 1
.Lcprio_L0:
.LBB0_608:
	s_cmp_lt_i32 s54, 5
	s_cselect_b64 s[2:3], -1, 0
	v_writelane_b32 v250, s2, 60
	s_and_b64 s[0:1], s[2:3], s[0:1]
	s_andn2_b64 vcc, exec, s[0:1]
	v_writelane_b32 v250, s3, 61
	v_writelane_b32 v250, s76, 62
	s_nop 1
	v_writelane_b32 v251, s78, 0
	v_writelane_b32 v251, s79, 1
	v_writelane_b32 v251, s80, 2
	v_writelane_b32 v251, s81, 3
	v_writelane_b32 v251, s82, 4
	v_writelane_b32 v251, s83, 5
	v_writelane_b32 v251, s84, 6
	v_writelane_b32 v251, s85, 7
	v_writelane_b32 v251, s86, 8
	v_writelane_b32 v251, s87, 9
	v_writelane_b32 v251, s88, 10
	v_writelane_b32 v251, s89, 11
	v_writelane_b32 v251, s90, 12
	v_writelane_b32 v250, s77, 63
	v_writelane_b32 v251, s91, 13
	s_cbranch_vccnz .LBB0_1086
	v_readlane_b32 s0, v250, 0
	v_mov_b32_e32 v182, v0
	s_mov_b32 s56, s0
	v_readlane_b32 s0, v250, 39
	v_readlane_b32 s1, v250, 1
	s_mov_b64 s[58:59], s[52:53]
	v_mov_b32_e32 v1, 1.0
	v_writelane_b32 v251, s1, 14
	s_mov_b64 s[0:1], s[90:91]
	v_mov_b32_e32 v164, 0x3f7b14be
	v_writelane_b32 v251, s58, 16
	v_mov_b32_e32 v165, 0x3f6c835e
	v_mov_b32_e32 v166, 0x3f54db31
	v_mov_b32_e32 v167, 0x3f3504f3
	v_mov_b32_e32 v168, 0x3f0e39da
	v_mov_b32_e32 v169, 0x3ec3ef15
	v_mov_b32_e32 v170, 0x3e47c5c2
	s_waitcnt vmcnt(9)
	v_mov_b32_e32 v11, 0
	v_mov_b32_e32 v171, 0
	s_cmpk_gt_i32 s56, 0x3ff
	v_writelane_b32 v251, s59, 17
	s_cbranch_scc1 .LBB0_942
	v_lshrrev_b32_e32 v2, 5, v182
	v_bitop3_b32 v173, v2, v182, 15 bitop3:0x6c
	v_ashrrev_i32_e32 v2, 1, v182
	v_and_b32_e32 v2, -16, v2
	v_lshl_add_u32 v176, v182, 4, v2
	v_add_u32_e32 v2, 0x200, v182
	v_cvt_f32_i32_e32 v3, v182
	v_ashrrev_i32_e32 v4, 1, v2
	v_and_b32_e32 v172, 15, v182
	v_ashrrev_i32_e32 v10, 4, v182
	s_movk_i32 s0, 0x210
	v_and_b32_e32 v4, -16, v4
	v_mul_lo_u32 v174, v10, s0
	v_lshl_add_u32 v177, v2, 4, v4
	v_cvt_f32_ubyte0_e32 v2, v172
	s_mov_b32 s0, 0x3b000000
	v_pk_mul_f32 v[4:5], v[2:3], -2.0 op_sel_hi:[1,0]
	s_mov_b32 s1, 0x38800000
	v_pk_mul_f32 v[4:5], v[4:5], s[0:1]
	s_mov_b32 s2, 0x7f800000
	v_and_b32_e32 v7, 0x7fffffff, v5
	v_and_b32_e32 v6, 0x7fffffff, v4
	v_pk_mul_f32 v[8:9], v[6:7], 0.5 op_sel_hi:[1,0]
	v_cmp_gt_f32_e64 s[0:1], |v5|, 1.0
	v_floor_f32_e32 v2, v9
	v_sub_f32_e32 v2, v9, v2
	v_min_f32_e32 v2, 0x3f7fffff, v2
	v_add_f32_e32 v2, v2, v2
	v_cmp_neq_f32_e32 vcc, s2, v9
	v_mov_b32_e32 v13, 0xbf1f24be
	v_xor_b32_e32 v7, v7, v5
	v_cndmask_b32_e32 v2, 0, v2, vcc
	v_cndmask_b32_e64 v2, |v5|, v2, s[0:1]
	v_add_f32_e32 v9, v2, v2
	v_rndne_f32_e32 v9, v9
	v_fmac_f32_e32 v2, -0.5, v9
	v_mul_f32_e32 v12, v2, v2
	s_waitcnt vmcnt(8)
	v_fmamk_f32 v14, v12, 0x3e75aa41, v13
	v_fmaak_f32 v14, v12, v14, 0x40234736
	v_fmaak_f32 v14, v12, v14, 0xc0a55e0e
	v_mul_f32_e32 v17, v2, v12
	v_mul_f32_e32 v14, v17, v14
	v_fmac_f32_e32 v14, 0x40490fdb, v2
	v_mov_b32_e32 v2, 0x3e642e9d
	v_cvt_i32_f32_e32 v9, v9
	v_fmamk_f32 v17, v12, 0x3d4be544, v2
	v_fmaak_f32 v17, v12, v17, 0xbfaad1da
	v_fmaak_f32 v17, v12, v17, 0x4081e0d3
	v_fmaak_f32 v17, v12, v17, 0xc09de9e6
	v_fma_f32 v12, v12, v17, 1.0
	v_lshlrev_b32_e32 v17, 30, v9
	v_and_b32_e32 v9, 1, v9
	v_cmp_eq_u32_e32 vcc, 0, v9
	s_movk_i32 s3, 0x1f8
	s_brev_b32 s45, 1
	v_cndmask_b32_e32 v9, v12, v14, vcc
	v_xor_b32_e32 v7, v7, v9
	v_xor_b32_e32 v9, 0x80000000, v14
	v_cndmask_b32_e32 v9, v9, v12, vcc
	v_cmp_class_f32_e64 vcc, v5, s3
	v_floor_f32_e32 v5, v8
	s_waitcnt vmcnt(7)
	v_and_b32_e32 v21, 0x80000000, v17
	v_sub_f32_e32 v5, v8, v5
	v_xor_b32_e32 v7, v7, v21
	v_bitop3_b32 v9, v9, v17, s45 bitop3:0x78
	v_mov_b32_e32 v12, 0x7fc00000
	v_min_f32_e32 v5, 0x3f7fffff, v5
	v_cndmask_b32_e32 v178, v12, v9, vcc
	v_cndmask_b32_e32 v179, v12, v7, vcc
	v_add_f32_e32 v5, v5, v5
	v_cmp_neq_f32_e32 vcc, s2, v8
	v_cmp_gt_f32_e64 s[0:1], |v4|, 1.0
	v_xor_b32_e32 v6, v6, v4
	v_cndmask_b32_e32 v5, 0, v5, vcc
	v_cndmask_b32_e64 v5, |v4|, v5, s[0:1]
	v_add_f32_e32 v7, v5, v5
	v_rndne_f32_e32 v7, v7
	v_fmac_f32_e32 v5, -0.5, v7
	v_mul_f32_e32 v8, v5, v5
	v_fmamk_f32 v9, v8, 0x3e75aa41, v13
	v_fmaak_f32 v9, v8, v9, 0x40234736
	v_fmaak_f32 v9, v8, v9, 0xc0a55e0e
	v_mul_f32_e32 v14, v5, v8
	v_mul_f32_e32 v9, v14, v9
	v_cvt_i32_f32_e32 v7, v7
	v_fmac_f32_e32 v9, 0x40490fdb, v5
	v_fmamk_f32 v5, v8, 0x3d4be544, v2
	v_fmaak_f32 v5, v8, v5, 0xbfaad1da
	v_fmaak_f32 v5, v8, v5, 0x4081e0d3
	v_fmaak_f32 v5, v8, v5, 0xc09de9e6
	v_fma_f32 v5, v8, v5, 1.0
	v_lshlrev_b32_e32 v8, 30, v7
	v_and_b32_e32 v7, 1, v7
	v_cmp_eq_u32_e32 vcc, 0, v7
	v_and_b32_e32 v14, 0x80000000, v8
	v_mul_f32_e32 v3, 0xb8800000, v3
	v_cndmask_b32_e32 v7, v5, v9, vcc
	v_xor_b32_e32 v6, v6, v7
	v_xor_b32_e32 v7, 0x80000000, v9
	v_cndmask_b32_e32 v5, v7, v5, vcc
	v_bitop3_b32 v5, v5, v8, s45 bitop3:0x78
	v_cmp_class_f32_e64 vcc, v4, s3
	v_xor_b32_e32 v6, v6, v14
	v_cmp_gt_f32_e64 s[0:1], |v3|, 1.0
	v_cndmask_b32_e32 v180, v12, v5, vcc
	v_mul_f32_e64 v5, |v3|, 0.5
	v_cndmask_b32_e32 v181, v12, v6, vcc
	v_fract_f32_e32 v6, v5
	v_add_f32_e32 v6, v6, v6
	v_cmp_neq_f32_e32 vcc, s2, v5
	s_ashr_i32 s57, s56, 31
	v_mov_b32_e32 v15, 0x40234736
	v_cndmask_b32_e32 v5, 0, v6, vcc
	v_cndmask_b32_e64 v5, |v3|, v5, s[0:1]
	s_lshl_b64 s[0:1], s[56:57], 18
	s_add_u32 s0, s58, s0
	s_addc_u32 s1, s59, s1
	s_add_u32 s46, s0, 0x2a940000
	s_addc_u32 s47, s1, 0
	s_add_u32 s64, s0, 0x2a960000
	v_add_f32_e32 v6, v5, v5
	s_addc_u32 s65, s1, 0
	v_rndne_f32_e32 v6, v6
	s_add_u32 s2, s58, 0x3f040000
	v_fmac_f32_e32 v5, -0.5, v6
	v_writelane_b32 v251, s2, 18
	s_addc_u32 s2, s59, 0
	v_mul_f32_e32 v7, v5, v5
	s_add_u32 s0, s0, 0x2a970000
	v_cvt_i32_f32_e32 v6, v6
	v_fmac_f32_e32 v13, 0x3e75aa41, v7
	v_writelane_b32 v251, s2, 20
	s_addc_u32 s1, s1, 0
	v_mov_b32_e32 v16, 0xc0a55e0e
	v_mov_b32_e32 v18, 0xbfaad1da
	v_fmac_f32_e32 v15, v7, v13
	v_fmac_f32_e32 v2, 0x3d4be544, v7
	v_writelane_b32 v251, s0, 22
	v_mov_b32_e32 v19, 0x4081e0d3
	v_fmac_f32_e32 v16, v7, v15
	v_mul_f32_e32 v8, v5, v7
	v_fmac_f32_e32 v18, v7, v2
	v_writelane_b32 v251, s1, 23
	s_add_u32 s0, s58, 0x22940000
	v_mov_b32_e32 v20, 0xc09de9e6
	v_mul_f32_e32 v8, v8, v16
	v_fmac_f32_e32 v19, v7, v18
	v_writelane_b32 v251, s0, 24
	s_addc_u32 s0, s59, 0
	v_fmac_f32_e32 v8, 0x40490fdb, v5
	v_fmac_f32_e32 v20, v7, v19
	v_lshlrev_b32_e32 v5, 30, v6
	v_and_b32_e32 v6, 1, v6
	v_writelane_b32 v251, s0, 26
	s_add_i32 s0, 0, 0x21000
	v_and_b32_e32 v4, 0x7fffffff, v3
	v_fma_f32 v2, v7, v20, 1.0
	v_cmp_eq_u32_e32 vcc, 0, v6
	v_writelane_b32 v251, s0, 28
	v_add_u32_e32 v186, s0, v10
	s_add_u32 s0, s58, 0x3af40000
	v_cndmask_b32_e32 v6, v2, v8, vcc
	v_xor_b32_e32 v4, v4, v3
	v_writelane_b32 v251, s0, 30
	s_addc_u32 s0, s59, 0
	s_mul_i32 s1, s56, 0x8200
	v_xor_b32_e32 v4, v4, v6
	v_xor_b32_e32 v6, 0x80000000, v8
	v_writelane_b32 v251, s0, 32
	s_mul_hi_i32 s0, s56, 0x8200
	s_add_u32 s1, s58, s1
	v_cndmask_b32_e32 v2, v6, v2, vcc
	s_addc_u32 s0, s59, s0
	v_bitop3_b32 v2, v2, v5, s45 bitop3:0x78
	v_cmp_class_f32_e64 vcc, v3, s3
	s_add_u32 s20, s1, 0x3f040800
	s_addc_u32 s21, s0, 0
	v_cndmask_b32_e32 v183, v12, v2, vcc
	v_and_b32_e32 v2, 63, v182
	s_add_i32 s0, 0, 0x21010
	v_writelane_b32 v251, s0, 34
	v_cmp_eq_u32_e64 s[0:1], 0, v2
	v_and_b32_e32 v7, 0x80000000, v5
	s_mov_b64 s[94:95], 0x3f800000
	v_writelane_b32 v251, s0, 36
	v_xor_b32_e32 v4, v4, v7
	v_mbcnt_lo_u32_b32 v3, -1, 0
	v_writelane_b32 v251, s1, 37
	s_mov_b32 s0, s56
	v_writelane_b32 v251, s0, 38
	v_bfe_u32 v175, v182, 1, 4
	v_cndmask_b32_e32 v184, v12, v4, vcc
	v_ashrrev_i32_e32 v185, 6, v182
	v_mov_b32_e32 v187, 0x3000
	v_mov_b32_e32 v188, 0x6000
	s_movk_i32 s22, 0x3fff
	s_movk_i32 s43, 0x4000
	s_movk_i32 s23, 0xfe00
	s_movk_i32 s48, 0xfc00
	s_movk_i32 s49, 0xfa00
	s_movk_i32 s50, 0xf800
	s_movk_i32 s51, 0xf600
	s_movk_i32 s57, 0xf400
	s_movk_i32 s58, 0xf200
	s_movk_i32 s59, 0xf000
	s_movk_i32 s78, 0x3000
	s_movk_i32 s60, 0xee00
	s_movk_i32 s61, 0xec00
	s_movk_i32 s62, 0xea00
	s_movk_i32 s63, 0xe800
	s_movk_i32 s66, 0xe600
	s_movk_i32 s67, 0xe400
	s_movk_i32 s68, 0xe200
	s_movk_i32 s69, 0xe000
	s_movk_i32 s74, 0xde00
	s_movk_i32 s75, 0xdc00
	s_movk_i32 s79, 0xda00
	s_movk_i32 s84, 0xce00
	s_mov_b32 s90, s45
	s_mov_b32 s91, s95
	v_mbcnt_hi_u32_b32 v189, -1, v3
	v_bfrev_b32_e32 v12, 1
	s_mov_b32 s97, -1.0
	v_writelane_b32 v251, s1, 39
	s_mov_b32 s24, s56
	s_movk_i32 s56, 0xd800
	s_movk_i32 s72, 0x4000
	s_movk_i32 s73, 0x7000
	s_branch .LBB0_612

.Lcprio_L1:
.LBB0_2704:
	s_cmp_lt_i32 s54, 17
	s_cselect_b64 s[2:3], -1, 0
	s_and_b64 s[0:1], s[2:3], s[0:1]
	s_andn2_b64 vcc, exec, s[0:1]
	s_cbranch_vccnz .LBB0_3118
	v_writelane_b32 v254, s2, 2
	v_readlane_b32 s1, v250, 1
	v_mov_b32_e32 v1, v0
	v_writelane_b32 v254, s3, 3
	s_mov_b32 s2, s1
	v_readlane_b32 s1, v250, 0
	s_waitcnt vmcnt(11)
	v_mov_b32_e32 v2, v248
	v_readlane_b32 s0, v250, 39
	s_mov_b32 s4, s1
	s_mov_b64 s[0:1], s[90:91]
	v_writelane_b32 v251, s2, 34
	s_mov_b64 s[2:3], s[52:53]
	s_cmpk_lt_i32 s4, 0x400
	v_writelane_b32 v254, s2, 0
	s_cselect_b64 s[0:1], -1, 0
	v_mov_b32_e32 v164, 1.0
	v_writelane_b32 v254, s3, 1
	v_writelane_b32 v254, s0, 4
	v_mov_b32_e32 v165, 0x3f7b14be
	v_mov_b32_e32 v166, 0x3f6c835e
	v_writelane_b32 v254, s1, 5
	s_mov_b32 s0, s4
	v_writelane_b32 v251, s0, 38
	v_mov_b32_e32 v167, 0x3f54db31
	v_mov_b32_e32 v168, 0x3f3504f3
	v_mov_b32_e32 v169, 0x3f0e39da
	v_mov_b32_e32 v170, 0x3ec3ef15
	v_mov_b32_e32 v171, 0x3e47c5c2
	s_waitcnt vmcnt(9)
	v_mov_b32_e32 v11, 0
	v_mov_b32_e32 v172, 0
	v_writelane_b32 v251, s1, 39
	s_cmpk_gt_i32 s4, 0x3ff
	s_cbranch_scc1 .LBB0_2986
	v_lshrrev_b32_e32 v2, 5, v1
	v_bitop3_b32 v174, v2, v1, 15 bitop3:0x6c
	v_ashrrev_i32_e32 v2, 1, v1
	v_and_b32_e32 v2, -16, v2
	v_lshl_add_u32 v178, v1, 4, v2
	v_add_u32_e32 v2, 0x200, v1
	v_cvt_f32_i32_e32 v3, v1
	v_ashrrev_i32_e32 v4, 1, v2
	v_and_b32_e32 v173, 15, v1
	v_ashrrev_i32_e32 v175, 4, v1
	s_movk_i32 s0, 0x210
	v_and_b32_e32 v4, -16, v4
	v_mul_lo_u32 v176, v175, s0
	v_lshl_add_u32 v179, v2, 4, v4
	v_cvt_f32_ubyte0_e32 v2, v173
	s_mov_b32 s0, 0x3b000000
	v_pk_mul_f32 v[4:5], v[2:3], -2.0 op_sel_hi:[1,0]
	s_mov_b32 s1, 0x38800000
	v_pk_mul_f32 v[4:5], v[4:5], s[0:1]
	s_mov_b32 s2, 0x7f800000
	v_and_b32_e32 v7, 0x7fffffff, v5
	v_and_b32_e32 v6, 0x7fffffff, v4
	v_pk_mul_f32 v[8:9], v[6:7], 0.5 op_sel_hi:[1,0]
	v_cmp_gt_f32_e64 s[0:1], |v5|, 1.0
	v_floor_f32_e32 v2, v9
	v_sub_f32_e32 v2, v9, v2
	v_min_f32_e32 v2, 0x3f7fffff, v2
	v_add_f32_e32 v2, v2, v2
	v_cmp_neq_f32_e32 vcc, s2, v9
	v_mov_b32_e32 v12, 0xbf1f24be
	v_xor_b32_e32 v7, v7, v5
	v_cndmask_b32_e32 v2, 0, v2, vcc
	v_cndmask_b32_e64 v2, |v5|, v2, s[0:1]
	v_add_f32_e32 v9, v2, v2
	v_rndne_f32_e32 v9, v9
	v_fmac_f32_e32 v2, -0.5, v9
	v_mul_f32_e32 v10, v2, v2
	v_fmamk_f32 v13, v10, 0x3e75aa41, v12
	v_fmaak_f32 v13, v10, v13, 0x40234736
	v_fmaak_f32 v13, v10, v13, 0xc0a55e0e
	s_waitcnt vmcnt(8)
	v_mul_f32_e32 v16, v2, v10
	v_mul_f32_e32 v13, v16, v13
	v_fmac_f32_e32 v13, 0x40490fdb, v2
	v_mov_b32_e32 v2, 0x3e642e9d
	v_cvt_i32_f32_e32 v9, v9
	v_fmamk_f32 v16, v10, 0x3d4be544, v2
	v_fmaak_f32 v16, v10, v16, 0xbfaad1da
	v_fmaak_f32 v16, v10, v16, 0x4081e0d3
	v_fmaak_f32 v16, v10, v16, 0xc09de9e6
	v_fma_f32 v10, v10, v16, 1.0
	v_lshlrev_b32_e32 v16, 30, v9
	v_and_b32_e32 v9, 1, v9
	v_cmp_eq_u32_e32 vcc, 0, v9
	s_movk_i32 s3, 0x1f8
	s_brev_b32 s47, 1
	v_cndmask_b32_e32 v9, v10, v13, vcc
	v_xor_b32_e32 v7, v7, v9
	v_xor_b32_e32 v9, 0x80000000, v13
	v_cndmask_b32_e32 v9, v9, v10, vcc
	v_cmp_class_f32_e64 vcc, v5, s3
	v_floor_f32_e32 v5, v8
	s_waitcnt vmcnt(7)
	v_and_b32_e32 v20, 0x80000000, v16
	v_sub_f32_e32 v5, v8, v5
	v_xor_b32_e32 v7, v7, v20
	v_bitop3_b32 v9, v9, v16, s47 bitop3:0x78
	v_mov_b32_e32 v10, 0x7fc00000
	v_min_f32_e32 v5, 0x3f7fffff, v5
	v_cndmask_b32_e32 v180, v10, v9, vcc
	v_cndmask_b32_e32 v181, v10, v7, vcc
	v_add_f32_e32 v5, v5, v5
	v_cmp_neq_f32_e32 vcc, s2, v8
	v_cmp_gt_f32_e64 s[0:1], |v4|, 1.0
	v_xor_b32_e32 v6, v6, v4
	v_cndmask_b32_e32 v5, 0, v5, vcc
	v_cndmask_b32_e64 v5, |v4|, v5, s[0:1]
	v_add_f32_e32 v7, v5, v5
	v_rndne_f32_e32 v7, v7
	v_fmac_f32_e32 v5, -0.5, v7
	v_mul_f32_e32 v8, v5, v5
	v_fmamk_f32 v9, v8, 0x3e75aa41, v12
	v_fmaak_f32 v9, v8, v9, 0x40234736
	v_fmaak_f32 v9, v8, v9, 0xc0a55e0e
	v_mul_f32_e32 v13, v5, v8
	v_mul_f32_e32 v9, v13, v9
	v_cvt_i32_f32_e32 v7, v7
	v_fmac_f32_e32 v9, 0x40490fdb, v5
	v_fmamk_f32 v5, v8, 0x3d4be544, v2
	v_fmaak_f32 v5, v8, v5, 0xbfaad1da
	v_fmaak_f32 v5, v8, v5, 0x4081e0d3
	v_fmaak_f32 v5, v8, v5, 0xc09de9e6
	v_fma_f32 v5, v8, v5, 1.0
	v_lshlrev_b32_e32 v8, 30, v7
	v_and_b32_e32 v7, 1, v7
	v_cmp_eq_u32_e32 vcc, 0, v7
	v_and_b32_e32 v13, 0x80000000, v8
	v_mul_f32_e32 v3, 0xb8800000, v3
	v_cndmask_b32_e32 v7, v5, v9, vcc
	v_xor_b32_e32 v6, v6, v7
	v_xor_b32_e32 v7, 0x80000000, v9
	v_cndmask_b32_e32 v5, v7, v5, vcc
	v_bitop3_b32 v5, v5, v8, s47 bitop3:0x78
	v_cmp_class_f32_e64 vcc, v4, s3
	v_xor_b32_e32 v6, v6, v13
	v_readlane_b32 s20, v251, 38
	v_cndmask_b32_e32 v182, v10, v5, vcc
	v_mul_f32_e64 v5, |v3|, 0.5
	v_cndmask_b32_e32 v183, v10, v6, vcc
	v_fract_f32_e32 v6, v5
	v_add_f32_e32 v6, v6, v6
	v_cmp_neq_f32_e32 vcc, s2, v5
	v_readlane_b32 s21, v251, 39
	v_cmp_gt_f32_e64 s[0:1], |v3|, 1.0
	v_cndmask_b32_e32 v5, 0, v6, vcc
	s_ashr_i32 s21, s20, 31
	v_cndmask_b32_e64 v5, |v3|, v5, s[0:1]
	s_lshl_b64 s[0:1], s[20:21], 18
	v_readlane_b32 s22, v254, 0
	v_readlane_b32 s23, v254, 1
	s_add_u32 s0, s22, s0
	s_addc_u32 s1, s23, s1
	s_add_u32 s48, s0, 0x2a940000
	s_addc_u32 s49, s1, 0
	s_add_u32 s66, s0, 0x2a960000
	v_add_f32_e32 v6, v5, v5
	s_addc_u32 s67, s1, 0
	v_readlane_b32 s4, v250, 23
	v_rndne_f32_e32 v6, v6
	v_readlane_b32 s5, v250, 24
	s_add_u32 s2, s4, 0x9000
	v_fmac_f32_e32 v5, -0.5, v6
	v_readlane_b32 s6, v250, 25
	v_writelane_b32 v251, s2, 52
	s_addc_u32 s2, s5, 0
	v_mul_f32_e32 v7, v5, v5
	v_readlane_b32 s7, v250, 26
	v_writelane_b32 v251, s2, 18
	s_add_u32 s2, s6, 0x3000
	v_mov_b32_e32 v14, 0x40234736
	v_cvt_i32_f32_e32 v6, v6
	v_fmac_f32_e32 v12, 0x3e75aa41, v7
	v_writelane_b32 v251, s2, 44
	s_addc_u32 s2, s7, 0
	v_mov_b32_e32 v15, 0xc0a55e0e
	v_mov_b32_e32 v17, 0xbfaad1da
	v_fmac_f32_e32 v14, v7, v12
	v_fmac_f32_e32 v2, 0x3d4be544, v7
	v_writelane_b32 v251, s2, 30
	s_add_u32 s2, s22, 0x3f040000
	v_mov_b32_e32 v18, 0x4081e0d3
	v_fmac_f32_e32 v15, v7, v14
	v_mul_f32_e32 v8, v5, v7
	v_fmac_f32_e32 v17, v7, v2
	v_readlane_b32 s8, v250, 27
	v_readlane_b32 s9, v250, 28
	v_readlane_b32 s10, v250, 29
	v_readlane_b32 s11, v250, 30
	v_readlane_b32 s12, v250, 31
	v_readlane_b32 s13, v250, 32
	v_readlane_b32 s14, v250, 33
	v_readlane_b32 s15, v250, 34
	v_readlane_b32 s16, v250, 35
	v_readlane_b32 s17, v250, 36
	v_readlane_b32 s18, v250, 37
	v_readlane_b32 s19, v250, 38
	v_writelane_b32 v250, s2, 23
	s_addc_u32 s2, s23, 0
	v_mov_b32_e32 v19, 0xc09de9e6
	v_mul_f32_e32 v8, v8, v15
	v_fmac_f32_e32 v18, v7, v17
	s_add_u32 s0, s0, 0x2a970000
	v_fmac_f32_e32 v8, 0x40490fdb, v5
	v_fmac_f32_e32 v19, v7, v18
	v_lshlrev_b32_e32 v5, 30, v6
	v_and_b32_e32 v6, 1, v6
	v_writelane_b32 v251, s2, 20
	s_addc_u32 s1, s1, 0
	v_and_b32_e32 v4, 0x7fffffff, v3
	v_fma_f32 v2, v7, v19, 1.0
	v_cmp_eq_u32_e32 vcc, 0, v6
	v_writelane_b32 v251, s0, 48
	v_xor_b32_e32 v4, v4, v3
	v_cndmask_b32_e32 v6, v2, v8, vcc
	v_writelane_b32 v251, s1, 49
	s_add_u32 s0, s22, 0x22940000
	v_xor_b32_e32 v4, v4, v6
	v_xor_b32_e32 v6, 0x80000000, v8
	v_writelane_b32 v251, s0, 22
	s_addc_u32 s0, s23, 0
	v_cndmask_b32_e32 v2, v6, v2, vcc
	v_cmp_class_f32_e64 vcc, v3, s3
	v_writelane_b32 v251, s0, 24
	v_readlane_b32 s0, v250, 44
	v_readlane_b32 s2, v250, 46
	v_readlane_b32 s3, v250, 47
	s_add_u32 s0, s2, 0x2000
	v_writelane_b32 v251, s0, 32
	s_addc_u32 s0, s3, 0
	v_readlane_b32 s1, v250, 45
	v_writelane_b32 v251, s0, 16
	s_add_u32 s0, s22, 0x3af40000
	v_writelane_b32 v251, s0, 54
	s_addc_u32 s0, s23, 0
	s_mul_i32 s1, s20, 0x8200
	v_readlane_b32 s4, v250, 48
	v_readlane_b32 s5, v250, 49
	v_readlane_b32 s6, v250, 50
	v_readlane_b32 s7, v250, 51
	v_readlane_b32 s8, v250, 52
	v_readlane_b32 s9, v250, 53
	v_readlane_b32 s10, v250, 54
	v_readlane_b32 s11, v250, 55
	v_readlane_b32 s12, v250, 56
	v_readlane_b32 s13, v250, 57
	v_readlane_b32 s14, v250, 58
	v_readlane_b32 s15, v250, 59
	v_writelane_b32 v250, s0, 60
	s_mul_hi_i32 s0, s20, 0x8200
	s_add_u32 s1, s22, s1
	s_addc_u32 s0, s23, s0
	v_bitop3_b32 v2, v2, v5, s47 bitop3:0x78
	s_add_u32 s6, s1, 0x3f040800
	v_cndmask_b32_e32 v184, v10, v2, vcc
	v_and_b32_e32 v2, 63, v1
	s_addc_u32 s7, s0, 0
	s_add_i32 s0, 0, 0x21010
	v_writelane_b32 v251, s0, 26
	v_cmp_eq_u32_e64 s[0:1], 0, v2
	v_and_b32_e32 v7, 0x80000000, v5
	s_mov_b64 s[42:43], 0x3f800000
	v_writelane_b32 v251, s0, 28
	v_xor_b32_e32 v4, v4, v7
	s_mov_b32 s68, 0x3f7ec46d
	v_writelane_b32 v251, s1, 29
	s_mov_b32 s0, s20
	s_mov_b32 s70, 0x3f7b14be
	s_mov_b32 s94, 0x3f6c835e
	v_mbcnt_lo_u32_b32 v3, -1, 0
	v_writelane_b32 v251, s0, 38
	v_bfe_u32 v177, v1, 1, 4
	v_cndmask_b32_e32 v185, v10, v4, vcc
	v_mov_b32_e32 v186, 0x3000
	v_mov_b32_e32 v187, 0x6000
	s_movk_i32 s10, 0x3fff
	s_movk_i32 s45, 0x4000
	s_movk_i32 s11, 0xfe00
	s_movk_i32 s50, 0xfc00
	s_movk_i32 s51, 0xfa00
	s_movk_i32 s56, 0xf800
	s_movk_i32 s57, 0xf600
	s_movk_i32 s58, 0xf400
	s_movk_i32 s59, 0xf200
	s_movk_i32 s60, 0xf000
	s_movk_i32 s61, 0x3000
	s_movk_i32 s62, 0xee00
	s_movk_i32 s63, 0xec00
	s_movk_i32 s64, 0xea00
	s_movk_i32 s65, 0xe800
	s_mov_b32 s69, 0xbdc8bd36
	s_mov_b32 s71, 0xbe47c5c2
	s_mov_b32 s95, 0xbec3ef15
	s_mov_b32 s92, s47
	s_mov_b32 s93, s43
	v_mbcnt_hi_u32_b32 v188, -1, v3
	v_bfrev_b32_e32 v12, 1
	s_movk_i32 s33, 0x7fff
	s_mov_b32 s77, -1.0
	v_writelane_b32 v251, s1, 39
	s_movk_i32 s90, 0x7000
	s_mov_b32 s91, 0xa000
	s_branch .LBB0_2708
